# topic loop with VGPR-bank-aware register assignment (split even/odd accumulators so fma sources hit distinct banks)
# speedup vs baseline: 1.0249x; 1.0216x over previous
.Ltopic_loop:
	v_add_u32_e32 v152, s0, v86
	ds_read_b128 v[136:139], v152
	ds_read_b128 v[140:143], v152 offset:32
	ds_read_b128 v[144:147], v152 offset:64
	ds_read_b128 v[148:151], v152 offset:96
	s_addk_i32 s0, 0x200
	s_waitcnt lgkmcnt(4)
	v_add_f32_e32 v104, v2, v88
	v_add_f32_e32 v108, v6, v88
	v_add_f32_e32 v112, v10, v88
	v_add_f32_e32 v116, v14, v88
	v_add_f32_e32 v105, v3, v89
	v_add_f32_e32 v109, v7, v89
	v_add_f32_e32 v113, v11, v89
	v_add_f32_e32 v117, v15, v89
	v_add_f32_e32 v106, v4, v90
	v_add_f32_e32 v110, v8, v90
	v_add_f32_e32 v114, v12, v90
	v_add_f32_e32 v118, v16, v90
	v_add_f32_e32 v107, v5, v91
	v_add_f32_e32 v111, v9, v91
	v_add_f32_e32 v115, v13, v91
	v_add_f32_e32 v119, v17, v91
	v_mul_f32_e32 v87, v66, v88
	v_fma_f32 v153, v66, |v104|, v82
	v_fma_f32 v155, v66, |v108|, v83
	v_fma_f32 v157, v66, |v112|, v84
	v_fma_f32 v159, v66, |v116|, v85
	v_mul_f32_e32 v166, v67, v89
	v_mul_f32_e64 v154, v67, |v105|
	v_mul_f32_e64 v156, v67, |v109|
	v_mul_f32_e64 v158, v67, |v113|
	v_mul_f32_e64 v164, v67, |v117|
	v_fmac_f32_e32 v87, v68, v90
	v_fma_f32 v153, v68, |v106|, v153
	v_fma_f32 v155, v68, |v110|, v155
	v_fma_f32 v157, v68, |v114|, v157
	v_fma_f32 v159, v68, |v118|, v159
	v_fmac_f32_e32 v166, v69, v91
	v_fma_f32 v154, v69, |v107|, v154
	v_fma_f32 v156, v69, |v111|, v156
	v_fma_f32 v158, v69, |v115|, v158
	v_fma_f32 v164, v69, |v119|, v164
	v_add_f32_e32 v120, v18, v92
	v_add_f32_e32 v124, v22, v92
	v_add_f32_e32 v128, v26, v92
	v_add_f32_e32 v132, v30, v92
	v_add_f32_e32 v121, v19, v93
	v_add_f32_e32 v125, v23, v93
	v_add_f32_e32 v129, v27, v93
	v_add_f32_e32 v133, v31, v93
	v_add_f32_e32 v122, v20, v94
	v_add_f32_e32 v126, v24, v94
	v_add_f32_e32 v130, v28, v94
	v_add_f32_e32 v134, v32, v94
	v_add_f32_e32 v123, v21, v95
	v_add_f32_e32 v127, v25, v95
	v_add_f32_e32 v131, v29, v95
	v_add_f32_e32 v135, v33, v95
	v_fmac_f32_e32 v87, v70, v92
	v_fma_f32 v153, v70, |v120|, v153
	v_fma_f32 v155, v70, |v124|, v155
	v_fma_f32 v157, v70, |v128|, v157
	v_fma_f32 v159, v70, |v132|, v159
	v_fmac_f32_e32 v166, v71, v93
	v_fma_f32 v154, v71, |v121|, v154
	v_fma_f32 v156, v71, |v125|, v156
	v_fma_f32 v158, v71, |v129|, v158
	v_fma_f32 v164, v71, |v133|, v164
	v_fmac_f32_e32 v87, v72, v94
	v_fma_f32 v153, v72, |v122|, v153
	v_fma_f32 v155, v72, |v126|, v155
	v_fma_f32 v157, v72, |v130|, v157
	v_fma_f32 v159, v72, |v134|, v159
	v_fmac_f32_e32 v166, v73, v95
	v_fma_f32 v154, v73, |v123|, v154
	v_fma_f32 v156, v73, |v127|, v156
	v_fma_f32 v158, v73, |v131|, v158
	v_fma_f32 v164, v73, |v135|, v164
	v_add_f32_e32 v104, v34, v96
	v_add_f32_e32 v108, v38, v96
	v_add_f32_e32 v112, v42, v96
	v_add_f32_e32 v116, v46, v96
	v_add_f32_e32 v105, v35, v97
	v_add_f32_e32 v109, v39, v97
	v_add_f32_e32 v113, v43, v97
	v_add_f32_e32 v117, v47, v97
	v_add_f32_e32 v106, v36, v98
	v_add_f32_e32 v110, v40, v98
	v_add_f32_e32 v114, v44, v98
	v_add_f32_e32 v118, v48, v98
	v_add_f32_e32 v107, v37, v99
	v_add_f32_e32 v111, v41, v99
	v_add_f32_e32 v115, v45, v99
	v_add_f32_e32 v119, v49, v99
	v_fmac_f32_e32 v87, v74, v96
	v_fma_f32 v153, v74, |v104|, v153
	v_fma_f32 v155, v74, |v108|, v155
	v_fma_f32 v157, v74, |v112|, v157
	v_fma_f32 v159, v74, |v116|, v159
	v_fmac_f32_e32 v166, v75, v97
	v_fma_f32 v154, v75, |v105|, v154
	v_fma_f32 v156, v75, |v109|, v156
	v_fma_f32 v158, v75, |v113|, v158
	v_fma_f32 v164, v75, |v117|, v164
	v_fmac_f32_e32 v87, v76, v98
	v_fma_f32 v153, v76, |v106|, v153
	v_fma_f32 v155, v76, |v110|, v155
	v_fma_f32 v157, v76, |v114|, v157
	v_fma_f32 v159, v76, |v118|, v159
	v_fmac_f32_e32 v166, v77, v99
	v_fma_f32 v154, v77, |v107|, v154
	v_fma_f32 v156, v77, |v111|, v156
	v_fma_f32 v158, v77, |v115|, v158
	v_fma_f32 v164, v77, |v119|, v164
	v_add_f32_e32 v120, v50, v100
	v_add_f32_e32 v124, v54, v100
	v_add_f32_e32 v128, v58, v100
	v_add_f32_e32 v132, v62, v100
	v_add_f32_e32 v121, v51, v101
	v_add_f32_e32 v125, v55, v101
	v_add_f32_e32 v129, v59, v101
	v_add_f32_e32 v133, v63, v101
	v_add_f32_e32 v122, v52, v102
	v_add_f32_e32 v126, v56, v102
	v_add_f32_e32 v130, v60, v102
	v_add_f32_e32 v134, v64, v102
	v_add_f32_e32 v123, v53, v103
	v_add_f32_e32 v127, v57, v103
	v_add_f32_e32 v131, v61, v103
	v_add_f32_e32 v135, v65, v103
	v_fmac_f32_e32 v87, v78, v100
	v_fma_f32 v153, v78, |v120|, v153
	v_fma_f32 v155, v78, |v124|, v155
	v_fma_f32 v157, v78, |v128|, v157
	v_fma_f32 v159, v78, |v132|, v159
	v_fmac_f32_e32 v166, v79, v101
	v_fma_f32 v154, v79, |v121|, v154
	v_fma_f32 v156, v79, |v125|, v156
	v_fma_f32 v158, v79, |v129|, v158
	v_fma_f32 v164, v79, |v133|, v164
	v_fmac_f32_e32 v87, v80, v102
	v_fma_f32 v153, v80, |v122|, v153
	v_fma_f32 v155, v80, |v126|, v155
	v_fma_f32 v157, v80, |v130|, v157
	v_fma_f32 v159, v80, |v134|, v159
	v_fmac_f32_e32 v166, v81, v103
	v_fma_f32 v154, v81, |v123|, v154
	v_fma_f32 v156, v81, |v127|, v156
	v_fma_f32 v158, v81, |v131|, v158
	v_fma_f32 v164, v81, |v135|, v164
	v_add_f32_e32 v87, v87, v166
	v_add_f32_e32 v153, v153, v154
	v_add_f32_e32 v155, v155, v156
	v_add_f32_e32 v157, v157, v158
	v_add_f32_e32 v159, v159, v164
	v_add_f32_e32 v153, v153, v87
	v_add_f32_e32 v155, v155, v87
	v_add_f32_e32 v157, v157, v87
	v_add_f32_e32 v159, v159, v87
	ds_write2_b32 v1, v153, v155 offset1:32
	ds_write2_b32 v1, v157, v159 offset0:64 offset1:96
	v_add_u32_e32 v1, 0x1000, v1
	v_add_u32_e32 v152, s0, v86
	ds_read_b128 v[88:91], v152
	ds_read_b128 v[92:95], v152 offset:32
	ds_read_b128 v[96:99], v152 offset:64
	ds_read_b128 v[100:103], v152 offset:96
	s_addk_i32 s0, 0x200
	s_waitcnt lgkmcnt(4)
	v_add_f32_e32 v104, v2, v136
	v_add_f32_e32 v108, v6, v136
	v_add_f32_e32 v112, v10, v136
	v_add_f32_e32 v116, v14, v136
	v_add_f32_e32 v105, v3, v137
	v_add_f32_e32 v109, v7, v137
	v_add_f32_e32 v113, v11, v137
	v_add_f32_e32 v117, v15, v137
	v_add_f32_e32 v106, v4, v138
	v_add_f32_e32 v110, v8, v138
	v_add_f32_e32 v114, v12, v138
	v_add_f32_e32 v118, v16, v138
	v_add_f32_e32 v107, v5, v139
	v_add_f32_e32 v111, v9, v139
	v_add_f32_e32 v115, v13, v139
	v_add_f32_e32 v119, v17, v139
	v_mul_f32_e32 v87, v66, v136
	v_fma_f32 v153, v66, |v104|, v82
	v_fma_f32 v155, v66, |v108|, v83
	v_fma_f32 v157, v66, |v112|, v84
	v_fma_f32 v159, v66, |v116|, v85
	v_mul_f32_e32 v166, v67, v137
	v_mul_f32_e64 v154, v67, |v105|
	v_mul_f32_e64 v156, v67, |v109|
	v_mul_f32_e64 v158, v67, |v113|
	v_mul_f32_e64 v164, v67, |v117|
	v_fmac_f32_e32 v87, v68, v138
	v_fma_f32 v153, v68, |v106|, v153
	v_fma_f32 v155, v68, |v110|, v155
	v_fma_f32 v157, v68, |v114|, v157
	v_fma_f32 v159, v68, |v118|, v159
	v_fmac_f32_e32 v166, v69, v139
	v_fma_f32 v154, v69, |v107|, v154
	v_fma_f32 v156, v69, |v111|, v156
	v_fma_f32 v158, v69, |v115|, v158
	v_fma_f32 v164, v69, |v119|, v164
	v_add_f32_e32 v120, v18, v140
	v_add_f32_e32 v124, v22, v140
	v_add_f32_e32 v128, v26, v140
	v_add_f32_e32 v132, v30, v140
	v_add_f32_e32 v121, v19, v141
	v_add_f32_e32 v125, v23, v141
	v_add_f32_e32 v129, v27, v141
	v_add_f32_e32 v133, v31, v141
	v_add_f32_e32 v122, v20, v142
	v_add_f32_e32 v126, v24, v142
	v_add_f32_e32 v130, v28, v142
	v_add_f32_e32 v134, v32, v142
	v_add_f32_e32 v123, v21, v143
	v_add_f32_e32 v127, v25, v143
	v_add_f32_e32 v131, v29, v143
	v_add_f32_e32 v135, v33, v143
	v_fmac_f32_e32 v87, v70, v140
	v_fma_f32 v153, v70, |v120|, v153
	v_fma_f32 v155, v70, |v124|, v155
	v_fma_f32 v157, v70, |v128|, v157
	v_fma_f32 v159, v70, |v132|, v159
	v_fmac_f32_e32 v166, v71, v141
	v_fma_f32 v154, v71, |v121|, v154
	v_fma_f32 v156, v71, |v125|, v156
	v_fma_f32 v158, v71, |v129|, v158
	v_fma_f32 v164, v71, |v133|, v164
	v_fmac_f32_e32 v87, v72, v142
	v_fma_f32 v153, v72, |v122|, v153
	v_fma_f32 v155, v72, |v126|, v155
	v_fma_f32 v157, v72, |v130|, v157
	v_fma_f32 v159, v72, |v134|, v159
	v_fmac_f32_e32 v166, v73, v143
	v_fma_f32 v154, v73, |v123|, v154
	v_fma_f32 v156, v73, |v127|, v156
	v_fma_f32 v158, v73, |v131|, v158
	v_fma_f32 v164, v73, |v135|, v164
	v_add_f32_e32 v104, v34, v144
	v_add_f32_e32 v108, v38, v144
	v_add_f32_e32 v112, v42, v144
	v_add_f32_e32 v116, v46, v144
	v_add_f32_e32 v105, v35, v145
	v_add_f32_e32 v109, v39, v145
	v_add_f32_e32 v113, v43, v145
	v_add_f32_e32 v117, v47, v145
	v_add_f32_e32 v106, v36, v146
	v_add_f32_e32 v110, v40, v146
	v_add_f32_e32 v114, v44, v146
	v_add_f32_e32 v118, v48, v146
	v_add_f32_e32 v107, v37, v147
	v_add_f32_e32 v111, v41, v147
	v_add_f32_e32 v115, v45, v147
	v_add_f32_e32 v119, v49, v147
	v_fmac_f32_e32 v87, v74, v144
	v_fma_f32 v153, v74, |v104|, v153
	v_fma_f32 v155, v74, |v108|, v155
	v_fma_f32 v157, v74, |v112|, v157
	v_fma_f32 v159, v74, |v116|, v159
	v_fmac_f32_e32 v166, v75, v145
	v_fma_f32 v154, v75, |v105|, v154
	v_fma_f32 v156, v75, |v109|, v156
	v_fma_f32 v158, v75, |v113|, v158
	v_fma_f32 v164, v75, |v117|, v164
	v_fmac_f32_e32 v87, v76, v146
	v_fma_f32 v153, v76, |v106|, v153
	v_fma_f32 v155, v76, |v110|, v155
	v_fma_f32 v157, v76, |v114|, v157
	v_fma_f32 v159, v76, |v118|, v159
	v_fmac_f32_e32 v166, v77, v147
	v_fma_f32 v154, v77, |v107|, v154
	v_fma_f32 v156, v77, |v111|, v156
	v_fma_f32 v158, v77, |v115|, v158
	v_fma_f32 v164, v77, |v119|, v164
	v_add_f32_e32 v120, v50, v148
	v_add_f32_e32 v124, v54, v148
	v_add_f32_e32 v128, v58, v148
	v_add_f32_e32 v132, v62, v148
	v_add_f32_e32 v121, v51, v149
	v_add_f32_e32 v125, v55, v149
	v_add_f32_e32 v129, v59, v149
	v_add_f32_e32 v133, v63, v149
	v_add_f32_e32 v122, v52, v150
	v_add_f32_e32 v126, v56, v150
	v_add_f32_e32 v130, v60, v150
	v_add_f32_e32 v134, v64, v150
	v_add_f32_e32 v123, v53, v151
	v_add_f32_e32 v127, v57, v151
	v_add_f32_e32 v131, v61, v151
	v_add_f32_e32 v135, v65, v151
	v_fmac_f32_e32 v87, v78, v148
	v_fma_f32 v153, v78, |v120|, v153
	v_fma_f32 v155, v78, |v124|, v155
	v_fma_f32 v157, v78, |v128|, v157
	v_fma_f32 v159, v78, |v132|, v159
	v_fmac_f32_e32 v166, v79, v149
	v_fma_f32 v154, v79, |v121|, v154
	v_fma_f32 v156, v79, |v125|, v156
	v_fma_f32 v158, v79, |v129|, v158
	v_fma_f32 v164, v79, |v133|, v164
	v_fmac_f32_e32 v87, v80, v150
	v_fma_f32 v153, v80, |v122|, v153
	v_fma_f32 v155, v80, |v126|, v155
	v_fma_f32 v157, v80, |v130|, v157
	v_fma_f32 v159, v80, |v134|, v159
	v_fmac_f32_e32 v166, v81, v151
	v_fma_f32 v154, v81, |v123|, v154
	v_fma_f32 v156, v81, |v127|, v156
	v_fma_f32 v158, v81, |v131|, v158
	v_fma_f32 v164, v81, |v135|, v164
	v_add_f32_e32 v87, v87, v166
	v_add_f32_e32 v153, v153, v154
	v_add_f32_e32 v155, v155, v156
	v_add_f32_e32 v157, v157, v158
	v_add_f32_e32 v159, v159, v164
	v_add_f32_e32 v153, v153, v87
	v_add_f32_e32 v155, v155, v87
	v_add_f32_e32 v157, v157, v87
	v_add_f32_e32 v159, v159, v87
	ds_write2_b32 v1, v153, v155 offset1:32
	ds_write2_b32 v1, v157, v159 offset0:64 offset1:96
	v_add_u32_e32 v1, 0x1000, v1
	s_cmpk_eq_i32 s0, 0x1600
	s_cbranch_scc0 .Ltopic_loop
	v_lshl_or_b32 v1, v227, 12, v226
	s_waitcnt lgkmcnt(0)
	s_barrier
	ds_read2st64_b32 v[2:3], v1 offset0:40 offset1:42
	ds_read2st64_b32 v[4:5], v1 offset0:44 offset1:46
	ds_read2st64_b32 v[6:7], v1 offset0:48 offset1:50
	v_or_b32_e32 v13, 16, v227
	s_waitcnt lgkmcnt(2)
	v_add_f32_e32 v2, s18, v2
	v_add_f32_e32 v8, v2, v3
	ds_read2st64_b32 v[2:3], v1 offset0:52 offset1:54
	s_waitcnt lgkmcnt(2)
	v_add_f32_e32 v4, v8, v4
	v_add_f32_e32 v4, v4, v5
	s_waitcnt lgkmcnt(1)
	v_add_f32_e32 v4, v4, v6
	v_add_f32_e32 v4, v4, v7
	s_waitcnt lgkmcnt(0)
	v_add_f32_e32 v2, v4, v2
	v_add_f32_e32 v2, v2, v3
	v_mul_f32_e32 v2, 0xbfb8aa3b, v2
	v_exp_f32_e32 v2, v2
	s_nop 0
	v_add_f32_e32 v4, 1.0, v2
	v_div_scale_f32 v5, s[0:1], v4, v4, 1.0
	v_rcp_f32_e32 v6, v5
	v_div_scale_f32 v7, vcc, 1.0, v4, 1.0
	ds_read2st64_b32 v[2:3], v1 offset0:104 offset1:106
	v_fma_f32 v8, -v5, v6, 1.0
	v_fmac_f32_e32 v6, v8, v6
	v_mul_f32_e32 v8, v7, v6
	v_fma_f32 v9, -v5, v8, v7
	v_fmac_f32_e32 v8, v9, v6
	v_fma_f32 v5, -v5, v8, v7
	v_div_fmas_f32 v5, v5, v6, v8
	v_div_fixup_f32 v8, v5, v4, 1.0
	ds_read2st64_b32 v[4:5], v1 offset0:108 offset1:110
	ds_read2st64_b32 v[6:7], v1 offset0:112 offset1:114
	s_waitcnt lgkmcnt(2)
	v_add_f32_e32 v2, s18, v2
	v_add_f32_e32 v9, v2, v3
	ds_read2st64_b32 v[2:3], v1 offset0:116 offset1:118
	s_waitcnt lgkmcnt(2)
	v_add_f32_e32 v4, v9, v4
	v_add_f32_e32 v4, v4, v5
	s_waitcnt lgkmcnt(1)
	v_add_f32_e32 v4, v4, v6
	v_add_f32_e32 v4, v4, v7
	s_waitcnt lgkmcnt(0)
	v_add_f32_e32 v2, v4, v2
	v_add_f32_e32 v2, v2, v3
	v_mul_f32_e32 v2, 0xbfb8aa3b, v2
	v_exp_f32_e32 v2, v2
	v_lshlrev_b32_e32 v3, 2, v227
	v_or_b32_e32 v6, 8, v227
	v_mov_b32_e32 v7, 0x17000
	v_add_f32_e32 v10, 1.0, v2
	v_div_scale_f32 v5, s[0:1], v10, v10, 1.0
	v_rcp_f32_e32 v11, v5
	v_or_b32_e32 v4, 0x17000, v3
	v_lshl_or_b32 v12, v6, 2, v7
	v_or_b32_e32 v2, 0x17010, v3
	v_or_b32_e32 v3, 0x17030, v3
	v_lshl_or_b32 v7, v13, 2, v7
	ds_read_b32 v4, v4
	ds_read_b32 v14, v2
	ds_read_b32 v12, v12
	ds_read_b32 v15, v3
	ds_read_b32 v16, v7
	s_waitcnt lgkmcnt(4)
	v_fmaak_f32 v2, v8, v4, 0xbc23d70a
	v_max_f32_e32 v8, 0, v2
	v_fma_f32 v2, -v5, v11, 1.0
	v_fmac_f32_e32 v11, v2, v11
	v_div_scale_f32 v4, vcc, 1.0, v10, 1.0
	v_mul_f32_e32 v17, v4, v11
	v_lshl_or_b32 v18, v6, 12, v226
	ds_read2st64_b32 v[2:3], v18 offset0:40 offset1:42
	v_fma_f32 v6, -v5, v17, v4
	v_fmac_f32_e32 v17, v6, v11
	v_fma_f32 v19, -v5, v17, v4
	ds_read2st64_b32 v[4:5], v18 offset0:44 offset1:46
	ds_read2st64_b32 v[6:7], v18 offset0:48 offset1:50
	s_waitcnt lgkmcnt(2)
	v_add_f32_e32 v2, s18, v2
	v_add_f32_e32 v20, v2, v3
	ds_read2st64_b32 v[2:3], v18 offset0:52 offset1:54
	s_waitcnt lgkmcnt(2)
	v_add_f32_e32 v4, v20, v4
	v_add_f32_e32 v4, v4, v5
	s_waitcnt lgkmcnt(1)
	v_add_f32_e32 v4, v4, v6
	v_add_f32_e32 v4, v4, v7
	s_waitcnt lgkmcnt(0)
	v_add_f32_e32 v2, v4, v2
	v_add_f32_e32 v2, v2, v3
	v_mul_f32_e32 v2, 0xbfb8aa3b, v2
	v_exp_f32_e32 v2, v2
	v_div_fmas_f32 v3, v19, v11, v17
	v_div_fixup_f32 v3, v3, v10, 1.0
	v_mov_b32_e32 v9, 0xbc23d70a
	v_add_f32_e32 v10, 1.0, v2
	v_div_scale_f32 v4, s[0:1], v10, v10, 1.0
	v_rcp_f32_e32 v11, v4
	v_fmaak_f32 v2, v3, v14, 0xbc23d70a
	v_max_f32_e32 v2, 0, v2
	v_add_f32_e32 v8, v8, v2
	v_fma_f32 v2, -v4, v11, 1.0
	v_fmac_f32_e32 v11, v2, v11
	v_div_scale_f32 v5, vcc, 1.0, v10, 1.0
	v_mul_f32_e32 v14, v5, v11
	ds_read2st64_b32 v[2:3], v1 offset0:232 offset1:234
	v_fma_f32 v6, -v4, v14, v5
	v_fmac_f32_e32 v14, v6, v11
	v_fma_f32 v17, -v4, v14, v5
	ds_read2st64_b32 v[4:5], v1 offset0:236 offset1:238
	ds_read2st64_b32 v[6:7], v1 offset0:240 offset1:242
	s_waitcnt lgkmcnt(2)
	v_add_f32_e32 v2, s18, v2
	v_add_f32_e32 v18, v2, v3
	ds_read2st64_b32 v[2:3], v1 offset0:244 offset1:246
	s_waitcnt lgkmcnt(2)
	v_add_f32_e32 v1, v18, v4
	v_add_f32_e32 v1, v1, v5
	s_waitcnt lgkmcnt(1)
	v_add_f32_e32 v1, v1, v6
	v_add_f32_e32 v1, v1, v7
	s_waitcnt lgkmcnt(0)
	v_add_f32_e32 v1, v1, v2
	v_add_f32_e32 v1, v1, v3
	v_mul_f32_e32 v1, 0xbfb8aa3b, v1
	v_exp_f32_e32 v1, v1
	v_div_fmas_f32 v2, v17, v11, v14
	v_div_fixup_f32 v2, v2, v10, 1.0
	v_fmaak_f32 v2, v2, v12, 0xbc23d70a
	v_add_f32_e32 v1, 1.0, v1
	v_div_scale_f32 v4, s[0:1], v1, v1, 1.0
	v_rcp_f32_e32 v10, v4
	v_max_f32_e32 v2, 0, v2
	v_add_f32_e32 v8, v8, v2
	v_div_scale_f32 v5, vcc, 1.0, v1, 1.0
	v_fma_f32 v2, -v4, v10, 1.0
	v_fmac_f32_e32 v10, v2, v10
	v_mul_f32_e32 v11, v5, v10
	v_lshl_or_b32 v12, v13, 12, v226
	ds_read2st64_b32 v[2:3], v12 offset0:40 offset1:42
	v_fma_f32 v6, -v4, v11, v5
	v_fmac_f32_e32 v11, v6, v10
	v_fma_f32 v13, -v4, v11, v5
	ds_read2st64_b32 v[4:5], v12 offset0:44 offset1:46
	ds_read2st64_b32 v[6:7], v12 offset0:48 offset1:50
	s_waitcnt lgkmcnt(2)
	v_add_f32_e32 v2, s18, v2
	v_add_f32_e32 v14, v2, v3
	ds_read2st64_b32 v[2:3], v12 offset0:52 offset1:54
	s_waitcnt lgkmcnt(2)
	v_add_f32_e32 v4, v14, v4
	v_add_f32_e32 v4, v4, v5
	s_waitcnt lgkmcnt(1)
	v_add_f32_e32 v4, v4, v6
	v_add_f32_e32 v4, v4, v7
	s_waitcnt lgkmcnt(0)
	v_add_f32_e32 v2, v4, v2
	v_add_f32_e32 v2, v2, v3
	v_mul_f32_e32 v2, 0xbfb8aa3b, v2
	v_exp_f32_e32 v2, v2
	v_div_fmas_f32 v3, v13, v10, v11
	v_div_fixup_f32 v1, v3, v1, 1.0
	v_fmaak_f32 v1, v1, v15, 0xbc23d70a
	v_add_f32_e32 v2, 1.0, v2
	v_div_scale_f32 v3, s[0:1], v2, v2, 1.0
	v_rcp_f32_e32 v4, v3
	v_max_f32_e32 v1, 0, v1
	v_add_f32_e32 v1, v8, v1
	s_lshl_b32 s0, s42, 5
	v_fma_f32 v5, -v3, v4, 1.0
	v_fmac_f32_e32 v4, v5, v4
	v_div_scale_f32 v5, vcc, 1.0, v2, 1.0
	v_mul_f32_e32 v6, v5, v4
	v_fma_f32 v7, -v3, v6, v5
	v_fmac_f32_e32 v6, v7, v4
	v_fma_f32 v3, -v3, v6, v5
	v_div_fmas_f32 v3, v3, v4, v6
	v_div_fixup_f32 v2, v3, v2, 1.0
	v_fmac_f32_e32 v9, v2, v16
	v_max_f32_e32 v2, 0, v9
	v_add_f32_e32 v2, v1, v2
	v_mov_b32_e32 v1, 0x16800
	v_lshl_or_b32 v1, v0, 2, v1
	v_cmp_gt_u32_e32 vcc, s0, v0
	ds_write_b32 v1, v2
	s_waitcnt lgkmcnt(0)
	s_barrier
	s_and_saveexec_b64 s[0:1], vcc
	s_cbranch_execz .LBB1_57
	ds_read2st64_b32 v[2:3], v1 offset1:2
	ds_read2st64_b32 v[4:5], v1 offset0:4 offset1:6
	v_add_u32_e32 v0, s33, v0
	v_ashrrev_i32_e32 v1, 31, v0
	v_lshl_add_u64 v[6:7], v[0:1], 2, s[10:11]
	s_waitcnt lgkmcnt(1)
	v_add_f32_e32 v1, v2, v3
	s_waitcnt lgkmcnt(0)
	v_add_f32_e32 v1, v1, v4
	v_add_f32_e32 v1, v1, v5
	v_add_u32_e32 v0, 0x7d00, v0
	v_mul_f32_e32 v2, 0x3d4ccccd, v1
	v_ashrrev_i32_e32 v1, 31, v0
	v_lshl_add_u64 v[0:1], v[0:1], 2, s[10:11]
	global_store_dword v[6:7], v2, off
	global_store_dword v[0:1], v2, off
